# i1 + grid barrier: workgroups that are not their XCD's last arriver poll the top-level generation word directly instead of waiting for their XCD leader to forward the release through the per-XCD word
# speedup vs baseline: 1.0257x; 1.0105x over previous
.LBB0_764:
	v_readlane_b32 s4, v243, 61
	v_readlane_b32 s5, v243, 62
	v_cvt_f32_u32_e32 v1, v4
	v_sub_u32_e32 v6, 0, v4
	v_rcp_iflag_f32_e32 v1, v1
	s_nop 1
	buffer_inv sc1
	global_atomic_add v5, v3, v216, s[4:5] sc0
	v_mul_f32_e32 v1, 0x4f7ffffe, v1
	v_cvt_u32_f32_e32 v1, v1
	v_mul_lo_u32 v6, v6, v1
	v_mul_hi_u32 v6, v1, v6
	v_add_u32_e32 v1, v1, v6
	s_waitcnt vmcnt(0)
	v_mul_hi_u32 v1, v5, v1
	v_mul_lo_u32 v6, v1, v4
	v_sub_u32_e32 v6, v5, v6
	v_add_u32_e32 v7, 1, v1
	v_cmp_ge_u32_e32 vcc, v6, v4
	v_add_u32_e32 v5, 1, v5
	s_nop 0
	v_cndmask_b32_e32 v1, v1, v7, vcc
	v_sub_u32_e32 v7, v6, v4
	v_cndmask_b32_e32 v6, v6, v7, vcc
	v_add_u32_e32 v7, 1, v1
	v_cmp_ge_u32_e32 vcc, v6, v4
	s_nop 1
	v_cndmask_b32_e32 v1, v1, v7, vcc
	v_mul_lo_u32 v6, v4, v1
	v_add_u32_e32 v4, v6, v4
	v_cmp_ne_u32_e32 vcc, v5, v4
	s_and_saveexec_b64 s[4:5], vcc
	s_xor_b64 s[4:5], exec, s[4:5]
	s_cbranch_execz .LBB0_778
	s_waitcnt lgkmcnt(0)
	v_readlane_b32 s98, v242, 1
	v_readlane_b32 s99, v242, 2
	s_nop 4
	global_load_dword v2, v3, s[98:99] sc1
	s_waitcnt vmcnt(0)
	v_cmp_eq_u32_e32 vcc, v2, v1
	s_and_saveexec_b64 s[6:7], vcc
	s_cbranch_execz .LBB0_777
	s_mov_b32 s19, 1
	s_mov_b64 s[8:9], 0
	s_branch .LBB0_768

.LBB0_770:
	global_load_dword v2, v3, s[98:99] sc1
	s_add_i32 s19, s19, 1
	s_mov_b64 s[14:15], -1
	s_waitcnt vmcnt(0)
	v_cmp_ne_u32_e32 vcc, v2, v1
	s_orn2_b64 s[12:13], vcc, exec
	s_branch .LBB0_767

.LBB0_2938:
	v_readlane_b32 s4, v243, 61
	v_readlane_b32 s5, v243, 62
	v_cvt_f32_u32_e32 v1, v4
	v_sub_u32_e32 v6, 0, v4
	v_rcp_iflag_f32_e32 v1, v1
	s_nop 1
	buffer_inv sc1
	global_atomic_add v5, v3, v216, s[4:5] sc0
	v_mul_f32_e32 v1, 0x4f7ffffe, v1
	v_cvt_u32_f32_e32 v1, v1
	v_mul_lo_u32 v6, v6, v1
	v_mul_hi_u32 v6, v1, v6
	v_add_u32_e32 v1, v1, v6
	s_waitcnt vmcnt(0)
	v_mul_hi_u32 v1, v5, v1
	v_mul_lo_u32 v6, v1, v4
	v_sub_u32_e32 v6, v5, v6
	v_add_u32_e32 v7, 1, v1
	v_cmp_ge_u32_e32 vcc, v6, v4
	v_add_u32_e32 v5, 1, v5
	s_nop 0
	v_cndmask_b32_e32 v1, v1, v7, vcc
	v_sub_u32_e32 v7, v6, v4
	v_cndmask_b32_e32 v6, v6, v7, vcc
	v_add_u32_e32 v7, 1, v1
	v_cmp_ge_u32_e32 vcc, v6, v4
	s_nop 1
	v_cndmask_b32_e32 v1, v1, v7, vcc
	v_mul_lo_u32 v6, v4, v1
	v_add_u32_e32 v4, v6, v4
	v_cmp_ne_u32_e32 vcc, v5, v4
	s_and_saveexec_b64 s[4:5], vcc
	s_xor_b64 s[4:5], exec, s[4:5]
	s_cbranch_execz .LBB0_2952
	s_waitcnt lgkmcnt(0)
	v_readlane_b32 s98, v242, 1
	v_readlane_b32 s99, v242, 2
	s_nop 4
	global_load_dword v2, v3, s[98:99] sc1
	s_waitcnt vmcnt(0)
	v_cmp_eq_u32_e32 vcc, v2, v1
	s_and_saveexec_b64 s[6:7], vcc
	s_cbranch_execz .LBB0_2951
	s_mov_b32 s18, 1
	s_mov_b64 s[8:9], 0
	s_branch .LBB0_2942

.LBB0_2944:
	global_load_dword v2, v3, s[98:99] sc1
	s_add_i32 s18, s18, 1
	s_mov_b64 s[14:15], -1
	s_waitcnt vmcnt(0)
	v_cmp_ne_u32_e32 vcc, v2, v1
	s_orn2_b64 s[12:13], vcc, exec
	s_branch .LBB0_2941
